# P1 K-loop: 3 of the 6 LDS-DMA issues of sub-phases 1 and 3 moved from the load segment into the following MFMA block (vmcnt 8->5 at those waits)
# speedup vs baseline: 1.0076x; 1.0076x over previous
; template <class Epi, bool GATHER, bool EXPERT, bool FP8>
; DI void gemm_phase(LAS unsigned char* lds, const Gemm g, const StaticOrder& S, const Epi& E) {
;     ...
;             const bool last = (t == nt - 2);
;             const char* a1 = cA + (size_t)(t + 1) * kstep;
;             const char* a2 = last ? nA : cA + (size_t)(t + 2) * kstep; const char* b2 = last ? nB : cB + (size_t)(t + 2) * kstep;
;             const char* a3 = a2 + kstep; const char* b3 = b2 + kstep;
.LBB0_115:
	ds_read_b128 v[130:133], v231
	ds_read_b128 v[134:137], v231 offset:1024
	ds_read_b128 v[138:141], v231 offset:2048
	ds_read_b128 v[142:145], v231 offset:3072
	ds_read_b128 v[146:149], v232
	ds_read_b128 v[150:153], v232 offset:1024
	ds_read_b128 v[154:157], v232 offset:2048
	ds_read_b128 v[158:161], v232 offset:3072
	s_add_u32 s0, s6, 0x80
	s_addc_u32 s1, s7, 0
	s_cmp_eq_u32 s18, 28
	s_cselect_b32 s9, s43, s1
	s_cselect_b32 s8, s42, s0
	s_cselect_b32 s1, s45, s15
	s_cselect_b32 s0, s44, s5
	v_mov_b32_e32 v186, v227
	ds_read_b128 v[162:165], v233
	ds_read_b128 v[166:169], v233 offset:1024
	ds_read_b128 v[170:173], v233 offset:2048
	ds_read_b128 v[174:177], v233 offset:3072
	ds_read_b128 v[178:181], v233 offset:4096
	ds_read_b128 v[182:185], v233 offset:5120
	ds_read_b128 v[192:195], v233 offset:6144
	ds_read_b128 v[196:199], v233 offset:7168
	s_add_i32 m0, s37, 0xc000
	s_nop 0
	global_load_lds_dwordx4 v186, s[6:7]
	v_mov_b32_e32 v186, v229
	s_add_i32 m0, s37, 0xe000
	s_nop 0
	global_load_lds_dwordx4 v186, s[6:7]
	s_waitcnt vmcnt(8)
	s_waitcnt lgkmcnt(0)
	s_barrier
	s_setprio 1
	s_waitcnt lgkmcnt(0)
	v_mfma_f32_16x16x32_bf16 v[126:129], v[130:133], v[162:165], v[126:129]
	v_mfma_f32_16x16x32_bf16 v[122:125], v[138:141], v[162:165], v[122:125]
	v_mfma_f32_16x16x32_bf16 v[118:121], v[130:133], v[170:173], v[118:121]
	v_mfma_f32_16x16x32_bf16 v[110:113], v[138:141], v[170:173], v[110:113]
	v_mfma_f32_16x16x32_bf16 v[102:105], v[130:133], v[178:181], v[102:105]
	v_mfma_f32_16x16x32_bf16 v[94:97], v[138:141], v[178:181], v[94:97]
	v_mfma_f32_16x16x32_bf16 v[86:89], v[130:133], v[192:195], v[86:89]
	v_mfma_f32_16x16x32_bf16 v[78:81], v[138:141], v[192:195], v[78:81]
	v_mfma_f32_16x16x32_bf16 v[126:129], v[134:137], v[166:169], v[126:129]
	v_mfma_f32_16x16x32_bf16 v[122:125], v[142:145], v[166:169], v[122:125]
	v_mfma_f32_16x16x32_bf16 v[118:121], v[134:137], v[174:177], v[118:121]
	v_mfma_f32_16x16x32_bf16 v[110:113], v[142:145], v[174:177], v[110:113]
	v_mfma_f32_16x16x32_bf16 v[102:105], v[134:137], v[182:185], v[102:105]
	v_mfma_f32_16x16x32_bf16 v[94:97], v[142:145], v[182:185], v[94:97]
	v_mfma_f32_16x16x32_bf16 v[86:89], v[134:137], v[196:199], v[86:89]
	v_mfma_f32_16x16x32_bf16 v[78:81], v[142:145], v[196:199], v[78:81]
	s_setprio 0
	s_setprio 1
	v_mfma_f32_16x16x32_bf16 v[114:117], v[146:149], v[162:165], v[114:117]
	v_mfma_f32_16x16x32_bf16 v[106:109], v[154:157], v[162:165], v[106:109]
	v_mfma_f32_16x16x32_bf16 v[98:101], v[146:149], v[170:173], v[98:101]
	v_mfma_f32_16x16x32_bf16 v[90:93], v[154:157], v[170:173], v[90:93]
	v_mfma_f32_16x16x32_bf16 v[82:85], v[146:149], v[178:181], v[82:85]
	v_mfma_f32_16x16x32_bf16 v[74:77], v[154:157], v[178:181], v[74:77]
	v_mfma_f32_16x16x32_bf16 v[70:73], v[146:149], v[192:195], v[70:73]
	v_mfma_f32_16x16x32_bf16 v[66:69], v[154:157], v[192:195], v[66:69]
	v_mfma_f32_16x16x32_bf16 v[114:117], v[150:153], v[166:169], v[114:117]
	v_mfma_f32_16x16x32_bf16 v[106:109], v[158:161], v[166:169], v[106:109]
	v_mfma_f32_16x16x32_bf16 v[98:101], v[150:153], v[174:177], v[98:101]
	v_mfma_f32_16x16x32_bf16 v[90:93], v[158:161], v[174:177], v[90:93]
	v_mfma_f32_16x16x32_bf16 v[82:85], v[150:153], v[182:185], v[82:85]
	v_mfma_f32_16x16x32_bf16 v[74:77], v[158:161], v[182:185], v[74:77]
	v_mfma_f32_16x16x32_bf16 v[70:73], v[150:153], v[196:199], v[70:73]
	v_mfma_f32_16x16x32_bf16 v[66:69], v[158:161], v[196:199], v[66:69]
	s_setprio 0
	s_barrier
	v_mov_b32_e32 v186, v1
	s_add_i32 s33, s75, s53
	ds_read_b128 v[162:165], v233 offset:16384
	ds_read_b128 v[166:169], v233 offset:17408
	ds_read_b128 v[170:173], v233 offset:18432
	ds_read_b128 v[174:177], v233 offset:19456
	ds_read_b128 v[178:181], v233 offset:20480
	ds_read_b128 v[182:185], v233 offset:21504
	ds_read_b128 v[192:195], v233 offset:22528
	ds_read_b128 v[196:199], v233 offset:23552
	s_mov_b32 m0, s33
	s_nop 0
	global_load_lds_dwordx4 v186, s[0:1]
	v_mov_b32_e32 v186, v225
	s_add_i32 m0, s33, 0x2000
	s_add_u32 s46, s0, 0x80000
	global_load_lds_dwordx4 v186, s[0:1]
	s_addc_u32 s47, s1, 0
	v_mov_b32_e32 v186, v1
	s_add_i32 s33, s76, s53
	s_mov_b32 m0, s33
	s_nop 0
	global_load_lds_dwordx4 v186, s[46:47]
	s_waitcnt vmcnt(5)
	s_waitcnt lgkmcnt(0)
	s_barrier
	s_setprio 1
	s_waitcnt lgkmcnt(0)
	v_mfma_f32_16x16x32_bf16 v[62:65], v[130:133], v[162:165], v[62:65]
	v_mfma_f32_16x16x32_bf16 v[58:61], v[138:141], v[162:165], v[58:61]
	v_mfma_f32_16x16x32_bf16 v[54:57], v[130:133], v[170:173], v[54:57]
	v_mfma_f32_16x16x32_bf16 v[46:49], v[138:141], v[170:173], v[46:49]
	v_mfma_f32_16x16x32_bf16 v[38:41], v[130:133], v[178:181], v[38:41]
	v_mfma_f32_16x16x32_bf16 v[30:33], v[138:141], v[178:181], v[30:33]
	v_mfma_f32_16x16x32_bf16 v[22:25], v[130:133], v[192:195], v[22:25]
	v_mfma_f32_16x16x32_bf16 v[14:17], v[138:141], v[192:195], v[14:17]
	v_mov_b32_e32 v186, v225
	s_add_i32 m0, s33, 0x2000
	s_nop 0
	global_load_lds_dwordx4 v186, s[46:47]
	v_mfma_f32_16x16x32_bf16 v[62:65], v[134:137], v[166:169], v[62:65]
	v_mfma_f32_16x16x32_bf16 v[58:61], v[142:145], v[166:169], v[58:61]
	v_mfma_f32_16x16x32_bf16 v[54:57], v[134:137], v[174:177], v[54:57]
	v_mfma_f32_16x16x32_bf16 v[46:49], v[142:145], v[174:177], v[46:49]
	v_mfma_f32_16x16x32_bf16 v[38:41], v[134:137], v[182:185], v[38:41]
	v_mfma_f32_16x16x32_bf16 v[30:33], v[142:145], v[182:185], v[30:33]
	v_mfma_f32_16x16x32_bf16 v[22:25], v[134:137], v[196:199], v[22:25]
	v_mfma_f32_16x16x32_bf16 v[14:17], v[142:145], v[196:199], v[14:17]
	v_mov_b32_e32 v186, v226
	s_mov_b32 m0, s37
	s_nop 0
	global_load_lds_dwordx4 v186, s[8:9]
	s_setprio 0
	s_setprio 1
	v_mfma_f32_16x16x32_bf16 v[50:53], v[146:149], v[162:165], v[50:53]
	v_mfma_f32_16x16x32_bf16 v[42:45], v[154:157], v[162:165], v[42:45]
	v_mfma_f32_16x16x32_bf16 v[34:37], v[146:149], v[170:173], v[34:37]
	v_mfma_f32_16x16x32_bf16 v[26:29], v[154:157], v[170:173], v[26:29]
	v_mfma_f32_16x16x32_bf16 v[18:21], v[146:149], v[178:181], v[18:21]
	v_mfma_f32_16x16x32_bf16 v[10:13], v[154:157], v[178:181], v[10:13]
	v_mfma_f32_16x16x32_bf16 v[6:9], v[146:149], v[192:195], v[6:9]
	v_mfma_f32_16x16x32_bf16 v[2:5], v[154:157], v[192:195], v[2:5]
	v_mov_b32_e32 v186, v228
	s_mov_b32 m0, s54
	s_nop 0
	global_load_lds_dwordx4 v186, s[8:9]
	v_mfma_f32_16x16x32_bf16 v[50:53], v[150:153], v[166:169], v[50:53]
	v_mfma_f32_16x16x32_bf16 v[42:45], v[158:161], v[166:169], v[42:45]
	v_mfma_f32_16x16x32_bf16 v[34:37], v[150:153], v[174:177], v[34:37]
	v_mfma_f32_16x16x32_bf16 v[26:29], v[158:161], v[174:177], v[26:29]
	v_mfma_f32_16x16x32_bf16 v[18:21], v[150:153], v[182:185], v[18:21]
	v_mfma_f32_16x16x32_bf16 v[10:13], v[158:161], v[182:185], v[10:13]
	v_mfma_f32_16x16x32_bf16 v[6:9], v[150:153], v[196:199], v[6:9]
	v_mfma_f32_16x16x32_bf16 v[2:5], v[158:161], v[196:199], v[2:5]
	s_setprio 0
	s_barrier
	s_add_i32 s33, 0, 0x18000
	s_add_i32 s39, 0, 0x1c000
	v_add_u32_e32 v142, s33, v230
	v_add_u32_e32 v158, s39, v230
	ds_read_b128 v[130:133], v142
	ds_read_b128 v[134:137], v142 offset:1024
	ds_read_b128 v[138:141], v142 offset:2048
	ds_read_b128 v[142:145], v142 offset:3072
	ds_read_b128 v[146:149], v158
	ds_read_b128 v[150:153], v158 offset:1024
	ds_read_b128 v[154:157], v158 offset:2048
	ds_read_b128 v[158:161], v158 offset:3072
	v_mov_b32_e32 v186, v227
	s_mov_b32 m0, s55
	ds_read_b128 v[162:165], v233 offset:32768
	ds_read_b128 v[166:169], v233 offset:33792
	ds_read_b128 v[170:173], v233 offset:34816
	ds_read_b128 v[174:177], v233 offset:35840
	ds_read_b128 v[178:181], v233 offset:36864
	ds_read_b128 v[182:185], v233 offset:37888
	ds_read_b128 v[192:195], v233 offset:38912
	ds_read_b128 v[196:199], v233 offset:39936
	s_nop 0
	global_load_lds_dwordx4 v186, s[8:9]
	v_mov_b32_e32 v186, v229
	s_mov_b32 m0, s56
	s_nop 0
	global_load_lds_dwordx4 v186, s[8:9]
	s_waitcnt vmcnt(8)
	s_waitcnt lgkmcnt(0)
	s_barrier
	s_setprio 1
	s_waitcnt lgkmcnt(0)
	v_mfma_f32_16x16x32_bf16 v[126:129], v[130:133], v[162:165], v[126:129]
	v_mfma_f32_16x16x32_bf16 v[122:125], v[138:141], v[162:165], v[122:125]
	v_mfma_f32_16x16x32_bf16 v[118:121], v[130:133], v[170:173], v[118:121]
	v_mfma_f32_16x16x32_bf16 v[110:113], v[138:141], v[170:173], v[110:113]
	v_mfma_f32_16x16x32_bf16 v[102:105], v[130:133], v[178:181], v[102:105]
	v_mfma_f32_16x16x32_bf16 v[94:97], v[138:141], v[178:181], v[94:97]
	v_mfma_f32_16x16x32_bf16 v[86:89], v[130:133], v[192:195], v[86:89]
	v_mfma_f32_16x16x32_bf16 v[78:81], v[138:141], v[192:195], v[78:81]
	v_mfma_f32_16x16x32_bf16 v[126:129], v[134:137], v[166:169], v[126:129]
	v_mfma_f32_16x16x32_bf16 v[122:125], v[142:145], v[166:169], v[122:125]
	v_mfma_f32_16x16x32_bf16 v[118:121], v[134:137], v[174:177], v[118:121]
	v_mfma_f32_16x16x32_bf16 v[110:113], v[142:145], v[174:177], v[110:113]
	v_mfma_f32_16x16x32_bf16 v[102:105], v[134:137], v[182:185], v[102:105]
	v_mfma_f32_16x16x32_bf16 v[94:97], v[142:145], v[182:185], v[94:97]
	v_mfma_f32_16x16x32_bf16 v[86:89], v[134:137], v[196:199], v[86:89]
	v_mfma_f32_16x16x32_bf16 v[78:81], v[142:145], v[196:199], v[78:81]
	s_setprio 0
	s_setprio 1
	v_mfma_f32_16x16x32_bf16 v[114:117], v[146:149], v[162:165], v[114:117]
	v_mfma_f32_16x16x32_bf16 v[106:109], v[154:157], v[162:165], v[106:109]
	v_mfma_f32_16x16x32_bf16 v[98:101], v[146:149], v[170:173], v[98:101]
	v_mfma_f32_16x16x32_bf16 v[90:93], v[154:157], v[170:173], v[90:93]
	v_mfma_f32_16x16x32_bf16 v[82:85], v[146:149], v[178:181], v[82:85]
	v_mfma_f32_16x16x32_bf16 v[74:77], v[154:157], v[178:181], v[74:77]
	v_mfma_f32_16x16x32_bf16 v[70:73], v[146:149], v[192:195], v[70:73]
	v_mfma_f32_16x16x32_bf16 v[66:69], v[154:157], v[192:195], v[66:69]
	v_mfma_f32_16x16x32_bf16 v[114:117], v[150:153], v[166:169], v[114:117]
	v_mfma_f32_16x16x32_bf16 v[106:109], v[158:161], v[166:169], v[106:109]
	v_mfma_f32_16x16x32_bf16 v[98:101], v[150:153], v[174:177], v[98:101]
	v_mfma_f32_16x16x32_bf16 v[90:93], v[158:161], v[174:177], v[90:93]
	v_mfma_f32_16x16x32_bf16 v[82:85], v[150:153], v[182:185], v[82:85]
	v_mfma_f32_16x16x32_bf16 v[74:77], v[158:161], v[182:185], v[74:77]
	v_mfma_f32_16x16x32_bf16 v[70:73], v[150:153], v[196:199], v[70:73]
	v_mfma_f32_16x16x32_bf16 v[66:69], v[158:161], v[196:199], v[66:69]
	s_setprio 0
	s_barrier
; template <class Epi, bool GATHER, bool EXPERT, bool FP8>
; DI void gemm_phase(LAS unsigned char* lds, const Gemm g, const StaticOrder& S, const Epi& E) {
;     ...
;         for (int t = 0; t < nt; t += 2) {
;             const bool last = (t == nt - 2);
;             const char* a1 = cA + (size_t)(t + 1) * kstep;
;             const char* a2 = last ? nA : cA + (size_t)(t + 2) * kstep; const char* b2 = last ? nB : cB + (size_t)(t + 2) * kstep;
;             const char* a3 = a2 + kstep; const char* b3 = b2 + kstep;
;             unsigned o00 = coffA[0][0], o01 = coffA[0][1], o10 = coffA[1][0], o11 = coffA[1][1];
;             if (GATHER && last && has_next) {
;                 o00 = sp[0] * (unsigned)(K * 2) + (unsigned)C0x2; o01 = sp[512] * (unsigned)(K * 2) + (unsigned)C1x2;
;                 o10 = sp[1024] * (unsigned)(K * 2) + (unsigned)C0x2; o11 = sp[1536] * (unsigned)(K * 2) + (unsigned)C1x2; }
;             PG8_TRIP(a1, a2, b2, a3, b3, o00, o01, o10, o11);
;             if (last) { coffA[0][0] = o00; coffA[0][1] = o01; coffA[1][0] = o10; coffA[1][1] = o11; }
;         }
	v_mov_b32_e32 v186, v1
	ds_read_b128 v[162:165], v233 offset:49152
	ds_read_b128 v[166:169], v233 offset:50176
	ds_read_b128 v[170:173], v233 offset:51200
	ds_read_b128 v[174:177], v233 offset:52224
	ds_read_b128 v[178:181], v233 offset:53248
	ds_read_b128 v[182:185], v233 offset:54272
	ds_read_b128 v[192:195], v233 offset:55296
	ds_read_b128 v[196:199], v233 offset:56320
	s_add_i32 s33, s33, s53
	v_lshl_add_u64 v[200:201], s[0:1], 0, v[186:187]
	v_lshl_add_u64 v[200:201], v[200:201], 0, s[24:25]
	s_mov_b32 m0, s33
	v_mov_b32_e32 v186, v225
	global_load_lds_dwordx4 v[200:201], off
	s_add_i32 m0, s33, 0x2000
	s_nop 0
	v_lshl_add_u64 v[200:201], s[0:1], 0, v[186:187]
	s_add_u32 s0, s0, 0x80080
	v_lshl_add_u64 v[200:201], v[200:201], 0, s[24:25]
	s_addc_u32 s1, s1, 0
	v_mov_b32_e32 v186, v1
	s_add_i32 s33, s39, s53
	global_load_lds_dwordx4 v[200:201], off
	s_mov_b32 m0, s33
	s_nop 0
	global_load_lds_dwordx4 v186, s[0:1]
	s_waitcnt vmcnt(5)
	s_waitcnt lgkmcnt(0)
	s_barrier
	s_setprio 1
	s_waitcnt lgkmcnt(0)
	v_mfma_f32_16x16x32_bf16 v[62:65], v[130:133], v[162:165], v[62:65]
	v_mfma_f32_16x16x32_bf16 v[58:61], v[138:141], v[162:165], v[58:61]
	v_mfma_f32_16x16x32_bf16 v[54:57], v[130:133], v[170:173], v[54:57]
	v_mfma_f32_16x16x32_bf16 v[46:49], v[138:141], v[170:173], v[46:49]
	v_mfma_f32_16x16x32_bf16 v[38:41], v[130:133], v[178:181], v[38:41]
	v_mfma_f32_16x16x32_bf16 v[30:33], v[138:141], v[178:181], v[30:33]
	v_mfma_f32_16x16x32_bf16 v[22:25], v[130:133], v[192:195], v[22:25]
	v_mfma_f32_16x16x32_bf16 v[14:17], v[138:141], v[192:195], v[14:17]
	v_mov_b32_e32 v186, v225
	s_add_i32 m0, s33, 0x2000
	s_nop 0
	global_load_lds_dwordx4 v186, s[0:1]
	v_mfma_f32_16x16x32_bf16 v[62:65], v[134:137], v[166:169], v[62:65]
	v_mfma_f32_16x16x32_bf16 v[58:61], v[142:145], v[166:169], v[58:61]
	v_mfma_f32_16x16x32_bf16 v[54:57], v[134:137], v[174:177], v[54:57]
	v_mfma_f32_16x16x32_bf16 v[46:49], v[142:145], v[174:177], v[46:49]
	v_mfma_f32_16x16x32_bf16 v[38:41], v[134:137], v[182:185], v[38:41]
	v_mfma_f32_16x16x32_bf16 v[30:33], v[142:145], v[182:185], v[30:33]
	v_mfma_f32_16x16x32_bf16 v[22:25], v[134:137], v[196:199], v[22:25]
	v_mfma_f32_16x16x32_bf16 v[14:17], v[142:145], v[196:199], v[14:17]
	v_mov_b32_e32 v186, v226
	s_mov_b32 m0, s62
	v_lshl_add_u64 v[200:201], s[8:9], 0, v[186:187]
	v_lshl_add_u64 v[200:201], v[200:201], 0, s[24:25]
	v_mov_b32_e32 v186, v228
	global_load_lds_dwordx4 v[200:201], off
	s_setprio 0
	s_setprio 1
	v_mfma_f32_16x16x32_bf16 v[50:53], v[146:149], v[162:165], v[50:53]
	v_mfma_f32_16x16x32_bf16 v[42:45], v[154:157], v[162:165], v[42:45]
	v_mfma_f32_16x16x32_bf16 v[34:37], v[146:149], v[170:173], v[34:37]
	v_mfma_f32_16x16x32_bf16 v[26:29], v[154:157], v[170:173], v[26:29]
	v_mfma_f32_16x16x32_bf16 v[18:21], v[146:149], v[178:181], v[18:21]
	v_mfma_f32_16x16x32_bf16 v[10:13], v[154:157], v[178:181], v[10:13]
	v_mfma_f32_16x16x32_bf16 v[6:9], v[146:149], v[192:195], v[6:9]
	v_mfma_f32_16x16x32_bf16 v[2:5], v[154:157], v[192:195], v[2:5]
	s_mov_b32 m0, s63
	v_lshl_add_u64 v[200:201], s[8:9], 0, v[186:187]
	v_lshl_add_u64 v[200:201], v[200:201], 0, s[24:25]
	global_load_lds_dwordx4 v[200:201], off
	v_mfma_f32_16x16x32_bf16 v[50:53], v[150:153], v[166:169], v[50:53]
	v_mfma_f32_16x16x32_bf16 v[42:45], v[158:161], v[166:169], v[42:45]
	v_mfma_f32_16x16x32_bf16 v[34:37], v[150:153], v[174:177], v[34:37]
	v_mfma_f32_16x16x32_bf16 v[26:29], v[158:161], v[174:177], v[26:29]
	v_mfma_f32_16x16x32_bf16 v[18:21], v[150:153], v[182:185], v[18:21]
	v_mfma_f32_16x16x32_bf16 v[10:13], v[158:161], v[182:185], v[10:13]
	v_mfma_f32_16x16x32_bf16 v[6:9], v[150:153], v[196:199], v[6:9]
	v_mfma_f32_16x16x32_bf16 v[2:5], v[158:161], v[196:199], v[2:5]
	s_setprio 0
	s_barrier
	s_add_i32 s18, s18, 2
	s_add_u32 s5, s5, 0x100
	s_addc_u32 s15, s15, 0
	s_add_u32 s6, s6, 0x100
	s_addc_u32 s7, s7, 0
	s_cmp_gt_u32 s18, 29
	s_cbranch_scc0 .LBB0_115
	s_and_b64 vcc, exec, s[26:27]
	s_cbranch_vccz .LBB0_118
	s_barrier
